# QK^T section: third K-fragment pair read up front into the spare register pair, fourth pair read where the third was; waits 4/2/2/0 so each wait has two MFMAs of distance
# baseline (speedup 1.0000x reference)
.LBB0_787:
	ds_read_b128 v[80:83], v134 offset:33792
	ds_read_b128 v[84:87], v134 offset:41984
	ds_read_b128 v[196:199], v135 offset:33792
	ds_read_b128 v[200:203], v135 offset:41984
	ds_read_b128 v[138:141], v136 offset:33792
	ds_read_b128 v[142:145], v136 offset:41984
	s_waitcnt lgkmcnt(4)
	v_mfma_f32_32x32x16_bf16 v[96:111], v[80:83], v[122:125], 0
	v_exp_f32_e32 v204, v72
	v_exp_f32_e32 v205, v73
	v_exp_f32_e32 v206, v74
	v_exp_f32_e32 v207, v75
	v_exp_f32_e32 v208, v76
	v_exp_f32_e32 v209, v77
	v_mfma_f32_32x32x16_bf16 v[80:95], v[84:87], v[122:125], 0
	v_exp_f32_e32 v210, v78
	v_exp_f32_e32 v79, v79
	s_waitcnt lgkmcnt(2)
	v_mfma_f32_32x32x16_bf16 v[96:111], v[196:199], v[126:129], v[96:111]
	v_mfma_f32_32x32x16_bf16 v[80:95], v[200:203], v[126:129], v[80:95]
	ds_read_b128 v[196:199], v137 offset:33792
	ds_read_b128 v[200:203], v137 offset:41984
	s_waitcnt lgkmcnt(2)
	v_mfma_f32_32x32x16_bf16 v[96:111], v[138:141], v[118:121], v[96:111]
	v_mfma_f32_32x32x16_bf16 v[80:95], v[142:145], v[118:121], v[80:95]
	v_exp_f32_e32 v180, v64
	v_add_f32_e32 v64, v161, v159
	v_add_f32_e32 v195, v157, v160
	v_add_f32_e32 v64, v155, v64
	v_add_f32_e32 v195, v158, v195
	v_add_f32_e32 v64, v154, v64
	v_add_f32_e32 v195, v156, v195
	v_add_f32_e32 v64, v151, v64
	v_add_f32_e32 v195, v153, v195
	v_add_f32_e32 v64, v149, v64
	v_add_f32_e32 v195, v152, v195
	v_add_f32_e32 v64, v147, v64
	s_waitcnt lgkmcnt(0)
	v_mfma_f32_32x32x16_bf16 v[96:111], v[196:199], v[114:117], v[96:111]
	v_exp_f32_e32 v197, v65
	v_add_f32_e32 v195, v150, v195
	v_exp_f32_e32 v198, v66
	v_add_f32_e32 v64, v146, v64
	v_exp_f32_e32 v199, v67
	v_add_f32_e32 v195, v148, v195
	v_add_f32_e32 v64, v180, v64
	v_mfma_f32_32x32x16_bf16 v[80:95], v[200:203], v[114:117], v[80:95]
	v_exp_f32_e32 v200, v68
	v_exp_f32_e32 v201, v69
	v_add_f32_e32 v195, v197, v195
	v_exp_f32_e32 v202, v70
	v_add_f32_e32 v64, v198, v64
	v_exp_f32_e32 v203, v71
	v_add_f32_e32 v195, v199, v195
	v_add_f32_e32 v64, v200, v64
	v_add_f32_e32 v195, v201, v195
	v_add_f32_e32 v64, v202, v64
	v_add_f32_e32 v195, v203, v195
	v_add_f32_e32 v64, v204, v64
	v_add_f32_e32 v195, v205, v195
	v_add_f32_e32 v64, v206, v64
	v_add_f32_e32 v195, v207, v195
	v_add_f32_e32 v64, v208, v64
	v_add_f32_e32 v195, v209, v195
	v_add_f32_e32 v64, v210, v64
	v_add_f32_e32 v195, v79, v195
	v_add_f32_e32 v195, v195, v64
	v_cvt_pk_bf16_f32 v64, v159, v161
	v_cvt_pk_bf16_f32 v65, v157, v160
	v_cvt_pk_bf16_f32 v66, v155, v158
	v_cvt_pk_bf16_f32 v67, v154, v156
	v_cvt_pk_bf16_f32 v68, v151, v153
	v_cvt_pk_bf16_f32 v69, v149, v152
	v_cvt_pk_bf16_f32 v70, v147, v150
	v_cvt_pk_bf16_f32 v71, v146, v148
	v_cvt_pk_bf16_f32 v72, v180, v197
	v_cvt_pk_bf16_f32 v73, v198, v199
	v_cvt_pk_bf16_f32 v74, v200, v201
	v_cvt_pk_bf16_f32 v75, v202, v203
	v_cvt_pk_bf16_f32 v76, v204, v205
	v_cvt_pk_bf16_f32 v77, v206, v207
	v_cvt_pk_bf16_f32 v78, v208, v209
	v_cvt_pk_bf16_f32 v79, v210, v79
	s_add_i32 m0, s84, 0x8400
	s_add_u32 s66, s78, s65
	s_addc_u32 s67, s79, 0
	global_load_lds_dwordx4 v185, s[66:67]
	s_add_i32 m0, s84, 0xa400
	s_add_i32 s64, s65, 0x60000
	global_load_lds_dwordx4 v184, s[66:67]
	s_add_i32 m0, s84, 0xc400
	s_add_u32 s70, s80, s64
	s_addc_u32 s71, s81, 0
	global_load_lds_dwordx4 v183, s[70:71]
	s_add_i32 m0, s84, 0xe400
	s_mov_b32 s65, s64
	global_load_lds_dwordx4 v182, s[70:71]
	ds_read_b64_tr_b16 v[198:199], v192 offset:1024
	ds_read_b64_tr_b16 v[200:201], v192 offset:3072
	ds_read_b64_tr_b16 v[202:203], v192 offset:5120
	ds_read_b64_tr_b16 v[204:205], v192 offset:7168
	ds_read_b64_tr_b16 v[206:207], v192 offset:9216
	ds_read_b64_tr_b16 v[208:209], v192 offset:11264
	ds_read_b64_tr_b16 v[222:223], v192 offset:13312
	ds_read_b64_tr_b16 v[224:225], v192 offset:15360
	s_waitcnt lgkmcnt(0)
	v_mfma_f32_32x32x16_bf16 v[0:15], v[64:67], v[198:201], v[0:15]
	ds_read_b64_tr_b16 v[198:199], v192 offset:1536
	ds_read_b64_tr_b16 v[200:201], v192 offset:3584
	ds_read_b64_tr_b16 v[138:139], v192 offset:9728
	ds_read_b64_tr_b16 v[140:141], v192 offset:11776
	v_mfma_f32_32x32x16_bf16 v[0:15], v[68:71], v[202:205], v[0:15]
	ds_read_b64_tr_b16 v[202:203], v192 offset:5632
	ds_read_b64_tr_b16 v[204:205], v192 offset:7680
	ds_read_b64_tr_b16 v[142:143], v192 offset:13824
	ds_read_b64_tr_b16 v[144:145], v192 offset:15872
	v_mfma_f32_32x32x16_bf16 v[0:15], v[72:75], v[206:209], v[0:15]
	v_mfma_f32_32x32x16_bf16 v[0:15], v[76:79], v[222:225], v[0:15]
	s_waitcnt lgkmcnt(0)
	v_mfma_f32_32x32x16_bf16 v[48:63], v[64:67], v[198:201], v[48:63]
	ds_read_b64_tr_b16 v[198:199], v192 offset:2048
	ds_read_b64_tr_b16 v[200:201], v192 offset:4096
	ds_read_b64_tr_b16 v[206:207], v192 offset:10240
	ds_read_b64_tr_b16 v[208:209], v192 offset:12288
	v_mfma_f32_32x32x16_bf16 v[48:63], v[68:71], v[202:205], v[48:63]
	ds_read_b64_tr_b16 v[202:203], v192 offset:6144
	ds_read_b64_tr_b16 v[204:205], v192 offset:8192
	ds_read_b64_tr_b16 v[222:223], v192 offset:14336
	ds_read_b64_tr_b16 v[224:225], v192 offset:16384
	v_mfma_f32_32x32x16_bf16 v[48:63], v[72:75], v[138:141], v[48:63]
	v_mfma_f32_32x32x16_bf16 v[48:63], v[76:79], v[142:145], v[48:63]
	s_waitcnt lgkmcnt(0)
	v_mfma_f32_32x32x16_bf16 v[32:47], v[64:67], v[198:201], v[32:47]
	ds_read_b64_tr_b16 v[198:199], v192 offset:2560
	ds_read_b64_tr_b16 v[200:201], v192 offset:4608
	ds_read_b64_tr_b16 v[138:139], v192 offset:10752
	ds_read_b64_tr_b16 v[140:141], v192 offset:12800
	v_mfma_f32_32x32x16_bf16 v[32:47], v[68:71], v[202:205], v[32:47]
	ds_read_b64_tr_b16 v[202:203], v192 offset:6656
	ds_read_b64_tr_b16 v[204:205], v192 offset:8704
	ds_read_b64_tr_b16 v[142:143], v192 offset:14848
	ds_read_b64_tr_b16 v[144:145], v192 offset:16896
	v_mfma_f32_32x32x16_bf16 v[32:47], v[72:75], v[206:209], v[32:47]
	v_mfma_f32_32x32x16_bf16 v[32:47], v[76:79], v[222:225], v[32:47]
	s_waitcnt lgkmcnt(0)
	v_mfma_f32_32x32x16_bf16 v[16:31], v[64:67], v[198:201], v[16:31]
	v_max_f32_e32 v64, v96, v97
	v_max3_f32 v65, v80, v81, v82
	v_max3_f32 v64, v64, v98, v99
	v_max3_f32 v65, v65, v83, v84
	v_max3_f32 v64, v64, v100, v101
	v_mfma_f32_32x32x16_bf16 v[16:31], v[68:71], v[202:205], v[16:31]
	v_max3_f32 v65, v65, v85, v86
	v_max3_f32 v64, v64, v102, v103
	v_max3_f32 v65, v65, v87, v88
	v_max3_f32 v64, v64, v104, v105
	v_max3_f32 v65, v65, v89, v90
	v_max3_f32 v64, v64, v106, v107
	v_max3_f32 v65, v65, v91, v92
	v_mfma_f32_32x32x16_bf16 v[16:31], v[72:75], v[138:141], v[16:31]
	v_max3_f32 v64, v64, v108, v109
	v_max3_f32 v65, v65, v93, v94
	v_max3_f32 v64, v64, v110, v111
	v_max3_f32 v64, v64, v65, v95
	v_mov_b32_e32 v198, 1.0
	v_mfma_f32_32x32x16_bf16 v[16:31], v[76:79], v[142:145], v[16:31]
	v_cmp_ge_f32_e64 s[0:1], s56, v64
	s_cmp_eq_u64 s[0:1], exec
	s_cbranch_scc1 .LBB0_792
	s_branch .LBB0_801

.LBB0_792:
	v_exp_f32_e32 v197, v96
	v_exp_f32_e32 v208, v97
	v_exp_f32_e32 v209, v98
	v_exp_f32_e32 v210, v99
	v_exp_f32_e32 v211, v100
	v_exp_f32_e32 v220, v101
	v_exp_f32_e32 v221, v102
	v_exp_f32_e32 v222, v103
	v_exp_f32_e32 v223, v104
	v_exp_f32_e32 v224, v105
	v_exp_f32_e32 v225, v106
	v_exp_f32_e32 v226, v107
	v_exp_f32_e32 v227, v108
	v_exp_f32_e32 v228, v109
	v_exp_f32_e32 v229, v110
	v_exp_f32_e32 v230, v111
	s_waitcnt vmcnt(4) lgkmcnt(0)
	s_barrier
	ds_read_b128 v[64:67], v134 offset:50176
	ds_read_b128 v[68:71], v134 offset:58368
	ds_read_b128 v[200:203], v135 offset:50176
	ds_read_b128 v[204:207], v135 offset:58368
	ds_read_b128 v[138:141], v136 offset:50176
	ds_read_b128 v[142:145], v136 offset:58368
	v_exp_f32_e32 v231, v87
	s_waitcnt lgkmcnt(4)
	v_mfma_f32_32x32x16_bf16 v[96:111], v[64:67], v[122:125], 0
	v_exp_f32_e32 v232, v88
	v_exp_f32_e32 v233, v89
	v_exp_f32_e32 v234, v90
	v_exp_f32_e32 v235, v91
	v_exp_f32_e32 v236, v92
	v_exp_f32_e32 v237, v93
	v_exp_f32_e32 v238, v94
	v_mfma_f32_32x32x16_bf16 v[64:79], v[68:71], v[122:125], 0
	v_exp_f32_e32 v95, v95
	s_waitcnt lgkmcnt(2)
	v_mfma_f32_32x32x16_bf16 v[96:111], v[200:203], v[126:129], v[96:111]
	v_mfma_f32_32x32x16_bf16 v[64:79], v[204:207], v[126:129], v[64:79]
	ds_read_b128 v[200:203], v137 offset:50176
	ds_read_b128 v[204:207], v137 offset:58368
	s_waitcnt lgkmcnt(2)
	v_mfma_f32_32x32x16_bf16 v[96:111], v[138:141], v[118:121], v[96:111]
	v_mfma_f32_32x32x16_bf16 v[64:79], v[142:145], v[118:121], v[64:79]
	s_waitcnt lgkmcnt(0)
	v_mfma_f32_32x32x16_bf16 v[96:111], v[200:203], v[114:117], v[96:111]
	v_exp_f32_e32 v201, v80
	v_add_f32_e32 v80, v208, v197
	v_add_f32_e32 v199, v209, v210
	v_add_f32_e32 v80, v211, v80
	v_add_f32_e32 v199, v220, v199
	v_add_f32_e32 v80, v221, v80
	v_add_f32_e32 v199, v222, v199
	v_add_f32_e32 v80, v223, v80
	v_add_f32_e32 v199, v224, v199
	v_add_f32_e32 v80, v225, v80
	v_add_f32_e32 v199, v226, v199
	v_add_f32_e32 v80, v227, v80
	v_exp_f32_e32 v202, v81
	v_add_f32_e32 v199, v228, v199
	v_exp_f32_e32 v203, v82
	v_add_f32_e32 v80, v229, v80
	v_mfma_f32_32x32x16_bf16 v[64:79], v[204:207], v[114:117], v[64:79]
	v_exp_f32_e32 v204, v83
	v_add_f32_e32 v199, v230, v199
	v_exp_f32_e32 v205, v84
	v_add_f32_e32 v80, v201, v80
	v_exp_f32_e32 v206, v85
	v_add_f32_e32 v199, v202, v199
	v_exp_f32_e32 v207, v86
	v_add_f32_e32 v80, v203, v80
	v_add_f32_e32 v199, v204, v199
	v_add_f32_e32 v80, v205, v80
	v_add_f32_e32 v199, v206, v199
	v_add_f32_e32 v80, v207, v80
	v_add_f32_e32 v199, v231, v199
	v_add_f32_e32 v80, v232, v80
	v_add_f32_e32 v199, v233, v199
	v_add_f32_e32 v80, v234, v80
	v_add_f32_e32 v199, v235, v199
	v_add_f32_e32 v80, v236, v80
	v_add_f32_e32 v199, v237, v199
	v_add_f32_e32 v80, v238, v80
	v_add_f32_e32 v199, v95, v199
	v_add_f32_e32 v199, v199, v80
	v_cvt_pk_bf16_f32 v80, v197, v208
	v_cvt_pk_bf16_f32 v81, v209, v210
	v_cvt_pk_bf16_f32 v82, v211, v220
	v_cvt_pk_bf16_f32 v83, v221, v222
	v_cvt_pk_bf16_f32 v84, v223, v224
	v_cvt_pk_bf16_f32 v85, v225, v226
	v_cvt_pk_bf16_f32 v86, v227, v228
	v_cvt_pk_bf16_f32 v87, v229, v230
	v_cvt_pk_bf16_f32 v88, v201, v202
	v_cvt_pk_bf16_f32 v89, v203, v204
	v_cvt_pk_bf16_f32 v90, v205, v206
	v_cvt_pk_bf16_f32 v91, v207, v231
	v_cvt_pk_bf16_f32 v92, v232, v233
	v_cvt_pk_bf16_f32 v93, v234, v235
	v_cvt_pk_bf16_f32 v94, v236, v237
	v_cvt_pk_bf16_f32 v95, v238, v95
	s_add_i32 m0, s84, 0x400
	s_add_u32 s66, s78, s65
	s_addc_u32 s67, s79, 0
	global_load_lds_dwordx4 v185, s[66:67]
	s_add_i32 m0, s84, 0x2400
	s_add_i32 s64, s65, 0x60000
	global_load_lds_dwordx4 v184, s[66:67]
	s_cmp_eq_u32 s55, 29
	s_cselect_b32 s64, s89, s64
	s_add_i32 m0, s84, 0x10400
	s_add_u32 s70, s80, s64
	s_addc_u32 s71, s81, 0
	global_load_lds_dwordx4 v183, s[70:71]
	s_add_i32 m0, s84, 0x12400
	s_mov_b32 s65, s64
	global_load_lds_dwordx4 v182, s[70:71]

.LBB0_799:
	v_exp_f32_e32 v159, v96
	v_exp_f32_e32 v161, v97
	v_exp_f32_e32 v157, v98
	v_exp_f32_e32 v160, v99
	v_exp_f32_e32 v155, v100
	v_exp_f32_e32 v158, v101
	v_exp_f32_e32 v154, v102
	v_exp_f32_e32 v156, v103
	v_exp_f32_e32 v151, v104
	v_exp_f32_e32 v153, v105
	v_exp_f32_e32 v149, v106
	v_exp_f32_e32 v152, v107
	v_exp_f32_e32 v147, v108
	v_exp_f32_e32 v150, v109
	v_exp_f32_e32 v146, v110
	v_exp_f32_e32 v148, v111
	v_fma_f32 v80, v193, v179, v195
	v_fma_f32 v179, v80, v198, v199
	s_cmp_gt_u32 s55, 32
	s_waitcnt vmcnt(4) lgkmcnt(0)
	s_barrier
	s_cbranch_scc1 .LBB0_803
	s_add_i32 s55, s55, 2
	v_mov_b32_e32 v193, v197
	ds_read_b128 v[80:83], v130 offset:50176
	ds_read_b128 v[84:87], v130 offset:58368
	ds_read_b128 v[196:199], v131 offset:50176
	ds_read_b128 v[200:203], v131 offset:58368
	ds_read_b128 v[138:141], v132 offset:50176
	ds_read_b128 v[142:145], v132 offset:58368
	s_waitcnt lgkmcnt(4)
	v_mfma_f32_32x32x16_bf16 v[96:111], v[80:83], v[122:125], 0
	v_exp_f32_e32 v204, v72
	v_exp_f32_e32 v205, v73
	v_exp_f32_e32 v206, v74
	v_exp_f32_e32 v207, v75
	v_exp_f32_e32 v208, v76
	v_exp_f32_e32 v209, v77
	v_mfma_f32_32x32x16_bf16 v[80:95], v[84:87], v[122:125], 0
	v_exp_f32_e32 v210, v78
	v_exp_f32_e32 v79, v79
	s_waitcnt lgkmcnt(2)
	v_mfma_f32_32x32x16_bf16 v[96:111], v[196:199], v[126:129], v[96:111]
	v_mfma_f32_32x32x16_bf16 v[80:95], v[200:203], v[126:129], v[80:95]
	ds_read_b128 v[196:199], v133 offset:50176
	ds_read_b128 v[200:203], v133 offset:58368
	s_waitcnt lgkmcnt(2)
	v_mfma_f32_32x32x16_bf16 v[96:111], v[138:141], v[118:121], v[96:111]
	v_mfma_f32_32x32x16_bf16 v[80:95], v[142:145], v[118:121], v[80:95]
	v_exp_f32_e32 v180, v64
	v_add_f32_e32 v64, v161, v159
	v_add_f32_e32 v195, v157, v160
	v_add_f32_e32 v64, v155, v64
	v_add_f32_e32 v195, v158, v195
	v_add_f32_e32 v64, v154, v64
	v_add_f32_e32 v195, v156, v195
	v_add_f32_e32 v64, v151, v64
	v_add_f32_e32 v195, v153, v195
	v_add_f32_e32 v64, v149, v64
	v_add_f32_e32 v195, v152, v195
	v_add_f32_e32 v64, v147, v64
	s_waitcnt lgkmcnt(0)
	v_mfma_f32_32x32x16_bf16 v[96:111], v[196:199], v[114:117], v[96:111]
	v_exp_f32_e32 v197, v65
	v_add_f32_e32 v195, v150, v195
	v_exp_f32_e32 v198, v66
	v_add_f32_e32 v64, v146, v64
	v_exp_f32_e32 v199, v67
	v_add_f32_e32 v195, v148, v195
	v_add_f32_e32 v64, v180, v64
	v_mfma_f32_32x32x16_bf16 v[80:95], v[200:203], v[114:117], v[80:95]
	v_exp_f32_e32 v200, v68
	v_exp_f32_e32 v201, v69
	v_add_f32_e32 v195, v197, v195
	v_exp_f32_e32 v202, v70
	v_add_f32_e32 v64, v198, v64
	v_exp_f32_e32 v203, v71
	v_add_f32_e32 v195, v199, v195
	v_add_f32_e32 v64, v200, v64
	v_add_f32_e32 v195, v201, v195
	v_add_f32_e32 v64, v202, v64
	v_add_f32_e32 v195, v203, v195
	v_add_f32_e32 v64, v204, v64
	v_add_f32_e32 v195, v205, v195
	v_add_f32_e32 v64, v206, v64
	v_add_f32_e32 v195, v207, v195
	v_add_f32_e32 v64, v208, v64
	v_add_f32_e32 v195, v209, v195
	v_add_f32_e32 v64, v210, v64
	v_add_f32_e32 v195, v79, v195
	v_add_f32_e32 v195, v195, v64
	v_cvt_pk_bf16_f32 v64, v159, v161
	v_cvt_pk_bf16_f32 v65, v157, v160
	v_cvt_pk_bf16_f32 v66, v155, v158
	v_cvt_pk_bf16_f32 v67, v154, v156
	v_cvt_pk_bf16_f32 v68, v151, v153
	v_cvt_pk_bf16_f32 v69, v149, v152
	v_cvt_pk_bf16_f32 v70, v147, v150
	v_cvt_pk_bf16_f32 v71, v146, v148
	v_cvt_pk_bf16_f32 v72, v180, v197
	v_cvt_pk_bf16_f32 v73, v198, v199
	v_cvt_pk_bf16_f32 v74, v200, v201
	v_cvt_pk_bf16_f32 v75, v202, v203
	v_cvt_pk_bf16_f32 v76, v204, v205
	v_cvt_pk_bf16_f32 v77, v206, v207
	v_cvt_pk_bf16_f32 v78, v208, v209
	v_cvt_pk_bf16_f32 v79, v210, v79
	s_add_i32 m0, s84, 0x4400
	s_add_u32 s66, s78, s65
	s_addc_u32 s67, s79, 0
	global_load_lds_dwordx4 v185, s[66:67]
	s_add_i32 m0, s84, 0x6400
	s_add_i32 s64, s65, 0x60000
	global_load_lds_dwordx4 v184, s[66:67]
	s_add_i32 m0, s84, 0x14400
	s_add_u32 s70, s80, s64
	s_addc_u32 s71, s81, 0
	global_load_lds_dwordx4 v183, s[70:71]
	s_add_i32 m0, s84, 0x16400
	s_mov_b32 s65, s64
	global_load_lds_dwordx4 v182, s[70:71]
	ds_read_b64_tr_b16 v[198:199], v192 offset:33792
	ds_read_b64_tr_b16 v[200:201], v192 offset:35840
	ds_read_b64_tr_b16 v[202:203], v192 offset:37888
	ds_read_b64_tr_b16 v[204:205], v192 offset:39936
	ds_read_b64_tr_b16 v[206:207], v192 offset:41984
	ds_read_b64_tr_b16 v[208:209], v192 offset:44032
	ds_read_b64_tr_b16 v[222:223], v192 offset:46080
	ds_read_b64_tr_b16 v[224:225], v192 offset:48128
	s_waitcnt lgkmcnt(0)
	v_mfma_f32_32x32x16_bf16 v[0:15], v[64:67], v[198:201], v[0:15]
	ds_read_b64_tr_b16 v[198:199], v192 offset:34304
	ds_read_b64_tr_b16 v[200:201], v192 offset:36352
	ds_read_b64_tr_b16 v[138:139], v192 offset:42496
	ds_read_b64_tr_b16 v[140:141], v192 offset:44544
	v_mfma_f32_32x32x16_bf16 v[0:15], v[68:71], v[202:205], v[0:15]
	ds_read_b64_tr_b16 v[202:203], v192 offset:38400
	ds_read_b64_tr_b16 v[204:205], v192 offset:40448
	ds_read_b64_tr_b16 v[142:143], v192 offset:46592
	ds_read_b64_tr_b16 v[144:145], v192 offset:48640
	v_mfma_f32_32x32x16_bf16 v[0:15], v[72:75], v[206:209], v[0:15]
	v_mfma_f32_32x32x16_bf16 v[0:15], v[76:79], v[222:225], v[0:15]
	s_waitcnt lgkmcnt(0)
	v_mfma_f32_32x32x16_bf16 v[48:63], v[64:67], v[198:201], v[48:63]
	ds_read_b64_tr_b16 v[198:199], v192 offset:34816
	ds_read_b64_tr_b16 v[200:201], v192 offset:36864
	ds_read_b64_tr_b16 v[206:207], v192 offset:43008
	ds_read_b64_tr_b16 v[208:209], v192 offset:45056
	v_mfma_f32_32x32x16_bf16 v[48:63], v[68:71], v[202:205], v[48:63]
	ds_read_b64_tr_b16 v[202:203], v192 offset:38912
	ds_read_b64_tr_b16 v[204:205], v192 offset:40960
	ds_read_b64_tr_b16 v[222:223], v192 offset:47104
	ds_read_b64_tr_b16 v[224:225], v192 offset:49152
	v_mfma_f32_32x32x16_bf16 v[48:63], v[72:75], v[138:141], v[48:63]
	v_mfma_f32_32x32x16_bf16 v[48:63], v[76:79], v[142:145], v[48:63]
	s_waitcnt lgkmcnt(0)
	v_mfma_f32_32x32x16_bf16 v[32:47], v[64:67], v[198:201], v[32:47]
	ds_read_b64_tr_b16 v[198:199], v192 offset:35328
	ds_read_b64_tr_b16 v[200:201], v192 offset:37376
	ds_read_b64_tr_b16 v[138:139], v192 offset:43520
	ds_read_b64_tr_b16 v[140:141], v192 offset:45568
	v_mfma_f32_32x32x16_bf16 v[32:47], v[68:71], v[202:205], v[32:47]
	ds_read_b64_tr_b16 v[202:203], v192 offset:39424
	ds_read_b64_tr_b16 v[204:205], v192 offset:41472
	ds_read_b64_tr_b16 v[142:143], v192 offset:47616
	ds_read_b64_tr_b16 v[144:145], v192 offset:49664
	v_mfma_f32_32x32x16_bf16 v[32:47], v[72:75], v[206:209], v[32:47]
	v_mfma_f32_32x32x16_bf16 v[32:47], v[76:79], v[222:225], v[32:47]
	s_waitcnt lgkmcnt(0)
	v_mfma_f32_32x32x16_bf16 v[16:31], v[64:67], v[198:201], v[16:31]
	v_max_f32_e32 v64, v96, v97
	v_max3_f32 v65, v80, v81, v82
	v_max3_f32 v64, v64, v98, v99
	v_max3_f32 v65, v65, v83, v84
	v_max3_f32 v64, v64, v100, v101
	v_mfma_f32_32x32x16_bf16 v[16:31], v[68:71], v[202:205], v[16:31]
	v_max3_f32 v65, v65, v85, v86
	v_max3_f32 v64, v64, v102, v103
	v_max3_f32 v65, v65, v87, v88
	v_max3_f32 v64, v64, v104, v105
	v_max3_f32 v65, v65, v89, v90
	v_max3_f32 v64, v64, v106, v107
	v_max3_f32 v65, v65, v91, v92
	v_mfma_f32_32x32x16_bf16 v[16:31], v[72:75], v[138:141], v[16:31]
	v_max3_f32 v64, v64, v108, v109
	v_max3_f32 v65, v65, v93, v94
	v_max3_f32 v64, v64, v110, v111
	v_max3_f32 v64, v64, v65, v95
	v_mov_b32_e32 v198, 1.0
	v_mfma_f32_32x32x16_bf16 v[16:31], v[76:79], v[142:145], v[16:31]
	v_cmp_ge_f32_e64 s[0:1], s56, v64
	s_cmp_eq_u64 s[0:1], exec
	s_cbranch_scc1 .Lc1_792
	s_branch .Lc1_801

.Lc1_792:
	v_exp_f32_e32 v197, v96
	v_exp_f32_e32 v208, v97
	v_exp_f32_e32 v209, v98
	v_exp_f32_e32 v210, v99
	v_exp_f32_e32 v211, v100
	v_exp_f32_e32 v220, v101
	v_exp_f32_e32 v221, v102
	v_exp_f32_e32 v222, v103
	v_exp_f32_e32 v223, v104
	v_exp_f32_e32 v224, v105
	v_exp_f32_e32 v225, v106
	v_exp_f32_e32 v226, v107
	v_exp_f32_e32 v227, v108
	v_exp_f32_e32 v228, v109
	v_exp_f32_e32 v229, v110
	v_exp_f32_e32 v230, v111
	s_waitcnt vmcnt(4) lgkmcnt(0)
	s_barrier
	ds_read_b128 v[64:67], v134 offset:33792
	ds_read_b128 v[68:71], v134 offset:41984
	ds_read_b128 v[200:203], v135 offset:33792
	ds_read_b128 v[204:207], v135 offset:41984
	ds_read_b128 v[138:141], v136 offset:33792
	ds_read_b128 v[142:145], v136 offset:41984
	v_exp_f32_e32 v231, v87
	s_waitcnt lgkmcnt(4)
	v_mfma_f32_32x32x16_bf16 v[96:111], v[64:67], v[122:125], 0
	v_exp_f32_e32 v232, v88
	v_exp_f32_e32 v233, v89
	v_exp_f32_e32 v234, v90
	v_exp_f32_e32 v235, v91
	v_exp_f32_e32 v236, v92
	v_exp_f32_e32 v237, v93
	v_exp_f32_e32 v238, v94
	v_mfma_f32_32x32x16_bf16 v[64:79], v[68:71], v[122:125], 0
	v_exp_f32_e32 v95, v95
	s_waitcnt lgkmcnt(2)
	v_mfma_f32_32x32x16_bf16 v[96:111], v[200:203], v[126:129], v[96:111]
	v_mfma_f32_32x32x16_bf16 v[64:79], v[204:207], v[126:129], v[64:79]
	ds_read_b128 v[200:203], v137 offset:33792
	ds_read_b128 v[204:207], v137 offset:41984
	s_waitcnt lgkmcnt(2)
	v_mfma_f32_32x32x16_bf16 v[96:111], v[138:141], v[118:121], v[96:111]
	v_mfma_f32_32x32x16_bf16 v[64:79], v[142:145], v[118:121], v[64:79]
	s_waitcnt lgkmcnt(0)
	v_mfma_f32_32x32x16_bf16 v[96:111], v[200:203], v[114:117], v[96:111]
	v_exp_f32_e32 v201, v80
	v_add_f32_e32 v80, v208, v197
	v_add_f32_e32 v199, v209, v210
	v_add_f32_e32 v80, v211, v80
	v_add_f32_e32 v199, v220, v199
	v_add_f32_e32 v80, v221, v80
	v_add_f32_e32 v199, v222, v199
	v_add_f32_e32 v80, v223, v80
	v_add_f32_e32 v199, v224, v199
	v_add_f32_e32 v80, v225, v80
	v_add_f32_e32 v199, v226, v199
	v_add_f32_e32 v80, v227, v80
	v_exp_f32_e32 v202, v81
	v_add_f32_e32 v199, v228, v199
	v_exp_f32_e32 v203, v82
	v_add_f32_e32 v80, v229, v80
	v_mfma_f32_32x32x16_bf16 v[64:79], v[204:207], v[114:117], v[64:79]
	v_exp_f32_e32 v204, v83
	v_add_f32_e32 v199, v230, v199
	v_exp_f32_e32 v205, v84
	v_add_f32_e32 v80, v201, v80
	v_exp_f32_e32 v206, v85
	v_add_f32_e32 v199, v202, v199
	v_exp_f32_e32 v207, v86
	v_add_f32_e32 v80, v203, v80
	v_add_f32_e32 v199, v204, v199
	v_add_f32_e32 v80, v205, v80
	v_add_f32_e32 v199, v206, v199
	v_add_f32_e32 v80, v207, v80
	v_add_f32_e32 v199, v231, v199
	v_add_f32_e32 v80, v232, v80
	v_add_f32_e32 v199, v233, v199
	v_add_f32_e32 v80, v234, v80
	v_add_f32_e32 v199, v235, v199
	v_add_f32_e32 v80, v236, v80
	v_add_f32_e32 v199, v237, v199
	v_add_f32_e32 v80, v238, v80
	v_add_f32_e32 v199, v95, v199
	v_add_f32_e32 v199, v199, v80
	v_cvt_pk_bf16_f32 v80, v197, v208
	v_cvt_pk_bf16_f32 v81, v209, v210
	v_cvt_pk_bf16_f32 v82, v211, v220
	v_cvt_pk_bf16_f32 v83, v221, v222
	v_cvt_pk_bf16_f32 v84, v223, v224
	v_cvt_pk_bf16_f32 v85, v225, v226
	v_cvt_pk_bf16_f32 v86, v227, v228
	v_cvt_pk_bf16_f32 v87, v229, v230
	v_cvt_pk_bf16_f32 v88, v201, v202
	v_cvt_pk_bf16_f32 v89, v203, v204
	v_cvt_pk_bf16_f32 v90, v205, v206
	v_cvt_pk_bf16_f32 v91, v207, v231
	v_cvt_pk_bf16_f32 v92, v232, v233
	v_cvt_pk_bf16_f32 v93, v234, v235
	v_cvt_pk_bf16_f32 v94, v236, v237
	v_cvt_pk_bf16_f32 v95, v238, v95
	s_add_i32 m0, s84, 0x8400
	s_add_u32 s66, s78, s65
	s_addc_u32 s67, s79, 0
	global_load_lds_dwordx4 v185, s[66:67]
	s_add_i32 m0, s84, 0xa400
	s_add_i32 s64, s65, 0x60000
	global_load_lds_dwordx4 v184, s[66:67]
	s_cmp_eq_u32 s55, 29
	s_cselect_b32 s64, s89, s64
	s_add_i32 m0, s84, 0xc400
	s_add_u32 s70, s80, s64
	s_addc_u32 s71, s81, 0
	global_load_lds_dwordx4 v183, s[70:71]
	s_add_i32 m0, s84, 0xe400
	s_mov_b32 s65, s64
	global_load_lds_dwordx4 v182, s[70:71]

.Lc1_799:
	v_exp_f32_e32 v159, v96
	v_exp_f32_e32 v161, v97
	v_exp_f32_e32 v157, v98
	v_exp_f32_e32 v160, v99
	v_exp_f32_e32 v155, v100
	v_exp_f32_e32 v158, v101
	v_exp_f32_e32 v154, v102
	v_exp_f32_e32 v156, v103
	v_exp_f32_e32 v151, v104
	v_exp_f32_e32 v153, v105
	v_exp_f32_e32 v149, v106
	v_exp_f32_e32 v152, v107
	v_exp_f32_e32 v147, v108
	v_exp_f32_e32 v150, v109
	v_exp_f32_e32 v146, v110
	v_exp_f32_e32 v148, v111
	v_fma_f32 v80, v193, v179, v195
	v_fma_f32 v179, v80, v198, v199
	s_cmp_gt_u32 s55, 32
	s_waitcnt vmcnt(4) lgkmcnt(0)
	s_barrier
	s_cbranch_scc1 .LBB0_803
	s_add_i32 s55, s55, 2
	v_mov_b32_e32 v193, v197
	ds_read_b128 v[80:83], v134 offset:50176
	ds_read_b128 v[84:87], v134 offset:58368
	ds_read_b128 v[196:199], v135 offset:50176
	ds_read_b128 v[200:203], v135 offset:58368
	ds_read_b128 v[138:141], v136 offset:50176
	ds_read_b128 v[142:145], v136 offset:58368
	s_waitcnt lgkmcnt(4)
	v_mfma_f32_32x32x16_bf16 v[96:111], v[80:83], v[122:125], 0
	v_exp_f32_e32 v204, v72
	v_exp_f32_e32 v205, v73
	v_exp_f32_e32 v206, v74
	v_exp_f32_e32 v207, v75
	v_exp_f32_e32 v208, v76
	v_exp_f32_e32 v209, v77
	v_mfma_f32_32x32x16_bf16 v[80:95], v[84:87], v[122:125], 0
	v_exp_f32_e32 v210, v78
	v_exp_f32_e32 v79, v79
	s_waitcnt lgkmcnt(2)
	v_mfma_f32_32x32x16_bf16 v[96:111], v[196:199], v[126:129], v[96:111]
	v_mfma_f32_32x32x16_bf16 v[80:95], v[200:203], v[126:129], v[80:95]
	ds_read_b128 v[196:199], v137 offset:50176
	ds_read_b128 v[200:203], v137 offset:58368
	s_waitcnt lgkmcnt(2)
	v_mfma_f32_32x32x16_bf16 v[96:111], v[138:141], v[118:121], v[96:111]
	v_mfma_f32_32x32x16_bf16 v[80:95], v[142:145], v[118:121], v[80:95]
	v_exp_f32_e32 v180, v64
	v_add_f32_e32 v64, v161, v159
	v_add_f32_e32 v195, v157, v160
	v_add_f32_e32 v64, v155, v64
	v_add_f32_e32 v195, v158, v195
	v_add_f32_e32 v64, v154, v64
	v_add_f32_e32 v195, v156, v195
	v_add_f32_e32 v64, v151, v64
	v_add_f32_e32 v195, v153, v195
	v_add_f32_e32 v64, v149, v64
	v_add_f32_e32 v195, v152, v195
	v_add_f32_e32 v64, v147, v64
	s_waitcnt lgkmcnt(0)
	v_mfma_f32_32x32x16_bf16 v[96:111], v[196:199], v[114:117], v[96:111]
	v_exp_f32_e32 v197, v65
	v_add_f32_e32 v195, v150, v195
	v_exp_f32_e32 v198, v66
	v_add_f32_e32 v64, v146, v64
	v_exp_f32_e32 v199, v67
	v_add_f32_e32 v195, v148, v195
	v_add_f32_e32 v64, v180, v64
	v_mfma_f32_32x32x16_bf16 v[80:95], v[200:203], v[114:117], v[80:95]
	v_exp_f32_e32 v200, v68
	v_exp_f32_e32 v201, v69
	v_add_f32_e32 v195, v197, v195
	v_exp_f32_e32 v202, v70
	v_add_f32_e32 v64, v198, v64
	v_exp_f32_e32 v203, v71
	v_add_f32_e32 v195, v199, v195
	v_add_f32_e32 v64, v200, v64
	v_add_f32_e32 v195, v201, v195
	v_add_f32_e32 v64, v202, v64
	v_add_f32_e32 v195, v203, v195
	v_add_f32_e32 v64, v204, v64
	v_add_f32_e32 v195, v205, v195
	v_add_f32_e32 v64, v206, v64
	v_add_f32_e32 v195, v207, v195
	v_add_f32_e32 v64, v208, v64
	v_add_f32_e32 v195, v209, v195
	v_add_f32_e32 v64, v210, v64
	v_add_f32_e32 v195, v79, v195
	v_add_f32_e32 v195, v195, v64
	v_cvt_pk_bf16_f32 v64, v159, v161
	v_cvt_pk_bf16_f32 v65, v157, v160
	v_cvt_pk_bf16_f32 v66, v155, v158
	v_cvt_pk_bf16_f32 v67, v154, v156
	v_cvt_pk_bf16_f32 v68, v151, v153
	v_cvt_pk_bf16_f32 v69, v149, v152
	v_cvt_pk_bf16_f32 v70, v147, v150
	v_cvt_pk_bf16_f32 v71, v146, v148
	v_cvt_pk_bf16_f32 v72, v180, v197
	v_cvt_pk_bf16_f32 v73, v198, v199
	v_cvt_pk_bf16_f32 v74, v200, v201
	v_cvt_pk_bf16_f32 v75, v202, v203
	v_cvt_pk_bf16_f32 v76, v204, v205
	v_cvt_pk_bf16_f32 v77, v206, v207
	v_cvt_pk_bf16_f32 v78, v208, v209
	v_cvt_pk_bf16_f32 v79, v210, v79
	s_add_i32 m0, s84, 0x400
	s_add_u32 s66, s78, s65
	s_addc_u32 s67, s79, 0
	global_load_lds_dwordx4 v185, s[66:67]
	s_add_i32 m0, s84, 0x2400
	s_add_i32 s64, s65, 0x60000
	global_load_lds_dwordx4 v184, s[66:67]
	s_add_i32 m0, s84, 0x10400
	s_add_u32 s70, s80, s64
	s_addc_u32 s71, s81, 0
	global_load_lds_dwordx4 v183, s[70:71]
	s_add_i32 m0, s84, 0x12400
	s_mov_b32 s65, s64
	global_load_lds_dwordx4 v182, s[70:71]
	ds_read_b64_tr_b16 v[198:199], v192 offset:17408
	ds_read_b64_tr_b16 v[200:201], v192 offset:19456
	ds_read_b64_tr_b16 v[202:203], v192 offset:21504
	ds_read_b64_tr_b16 v[204:205], v192 offset:23552
	ds_read_b64_tr_b16 v[206:207], v192 offset:25600
	ds_read_b64_tr_b16 v[208:209], v192 offset:27648
	ds_read_b64_tr_b16 v[222:223], v192 offset:29696
	ds_read_b64_tr_b16 v[224:225], v192 offset:31744
	s_waitcnt lgkmcnt(0)
	v_mfma_f32_32x32x16_bf16 v[0:15], v[64:67], v[198:201], v[0:15]
	ds_read_b64_tr_b16 v[198:199], v192 offset:17920
	ds_read_b64_tr_b16 v[200:201], v192 offset:19968
	ds_read_b64_tr_b16 v[138:139], v192 offset:26112
	ds_read_b64_tr_b16 v[140:141], v192 offset:28160
	v_mfma_f32_32x32x16_bf16 v[0:15], v[68:71], v[202:205], v[0:15]
	ds_read_b64_tr_b16 v[202:203], v192 offset:22016
	ds_read_b64_tr_b16 v[204:205], v192 offset:24064
	ds_read_b64_tr_b16 v[142:143], v192 offset:30208
	ds_read_b64_tr_b16 v[144:145], v192 offset:32256
	v_mfma_f32_32x32x16_bf16 v[0:15], v[72:75], v[206:209], v[0:15]
	v_mfma_f32_32x32x16_bf16 v[0:15], v[76:79], v[222:225], v[0:15]
	s_waitcnt lgkmcnt(0)
	v_mfma_f32_32x32x16_bf16 v[48:63], v[64:67], v[198:201], v[48:63]
	ds_read_b64_tr_b16 v[198:199], v192 offset:18432
	ds_read_b64_tr_b16 v[200:201], v192 offset:20480
	ds_read_b64_tr_b16 v[206:207], v192 offset:26624
	ds_read_b64_tr_b16 v[208:209], v192 offset:28672
	v_mfma_f32_32x32x16_bf16 v[48:63], v[68:71], v[202:205], v[48:63]
	ds_read_b64_tr_b16 v[202:203], v192 offset:22528
	ds_read_b64_tr_b16 v[204:205], v192 offset:24576
	ds_read_b64_tr_b16 v[222:223], v192 offset:30720
	ds_read_b64_tr_b16 v[224:225], v192 offset:32768
	v_mfma_f32_32x32x16_bf16 v[48:63], v[72:75], v[138:141], v[48:63]
	v_mfma_f32_32x32x16_bf16 v[48:63], v[76:79], v[142:145], v[48:63]
	s_waitcnt lgkmcnt(0)
	v_mfma_f32_32x32x16_bf16 v[32:47], v[64:67], v[198:201], v[32:47]
	ds_read_b64_tr_b16 v[198:199], v192 offset:18944
	ds_read_b64_tr_b16 v[200:201], v192 offset:20992
	ds_read_b64_tr_b16 v[138:139], v192 offset:27136
	ds_read_b64_tr_b16 v[140:141], v192 offset:29184
	v_mfma_f32_32x32x16_bf16 v[32:47], v[68:71], v[202:205], v[32:47]
	ds_read_b64_tr_b16 v[202:203], v192 offset:23040
	ds_read_b64_tr_b16 v[204:205], v192 offset:25088
	ds_read_b64_tr_b16 v[142:143], v192 offset:31232
	ds_read_b64_tr_b16 v[144:145], v192 offset:33280
	v_mfma_f32_32x32x16_bf16 v[32:47], v[72:75], v[206:209], v[32:47]
	v_mfma_f32_32x32x16_bf16 v[32:47], v[76:79], v[222:225], v[32:47]
	s_waitcnt lgkmcnt(0)
	v_mfma_f32_32x32x16_bf16 v[16:31], v[64:67], v[198:201], v[16:31]
	v_max_f32_e32 v64, v96, v97
	v_max3_f32 v65, v80, v81, v82
	v_max3_f32 v64, v64, v98, v99
	v_max3_f32 v65, v65, v83, v84
	v_max3_f32 v64, v64, v100, v101
	v_mfma_f32_32x32x16_bf16 v[16:31], v[68:71], v[202:205], v[16:31]
	v_max3_f32 v65, v65, v85, v86
	v_max3_f32 v64, v64, v102, v103
	v_max3_f32 v65, v65, v87, v88
	v_max3_f32 v64, v64, v104, v105
	v_max3_f32 v65, v65, v89, v90
	v_max3_f32 v64, v64, v106, v107
	v_max3_f32 v65, v65, v91, v92
	v_mfma_f32_32x32x16_bf16 v[16:31], v[72:75], v[138:141], v[16:31]
	v_max3_f32 v64, v64, v108, v109
	v_max3_f32 v65, v65, v93, v94
	v_max3_f32 v64, v64, v110, v111
	v_max3_f32 v64, v64, v65, v95
	v_mov_b32_e32 v198, 1.0
	v_mfma_f32_32x32x16_bf16 v[16:31], v[76:79], v[142:145], v[16:31]
	v_cmp_ge_f32_e64 s[0:1], s56, v64
	s_cmp_eq_u64 s[0:1], exec
	s_cbranch_scc1 .Lc2_792
	s_branch .Lc2_801

.Lc2_792:
	v_exp_f32_e32 v197, v96
	v_exp_f32_e32 v208, v97
	v_exp_f32_e32 v209, v98
	v_exp_f32_e32 v210, v99
	v_exp_f32_e32 v211, v100
	v_exp_f32_e32 v220, v101
	v_exp_f32_e32 v221, v102
	v_exp_f32_e32 v222, v103
	v_exp_f32_e32 v223, v104
	v_exp_f32_e32 v224, v105
	v_exp_f32_e32 v225, v106
	v_exp_f32_e32 v226, v107
	v_exp_f32_e32 v227, v108
	v_exp_f32_e32 v228, v109
	v_exp_f32_e32 v229, v110
	v_exp_f32_e32 v230, v111
	s_waitcnt vmcnt(4) lgkmcnt(0)
	s_barrier
	ds_read_b128 v[64:67], v130 offset:50176
	ds_read_b128 v[68:71], v130 offset:58368
	ds_read_b128 v[200:203], v131 offset:50176
	ds_read_b128 v[204:207], v131 offset:58368
	ds_read_b128 v[138:141], v132 offset:50176
	ds_read_b128 v[142:145], v132 offset:58368
	v_exp_f32_e32 v231, v87
	s_waitcnt lgkmcnt(4)
	v_mfma_f32_32x32x16_bf16 v[96:111], v[64:67], v[122:125], 0
	v_exp_f32_e32 v232, v88
	v_exp_f32_e32 v233, v89
	v_exp_f32_e32 v234, v90
	v_exp_f32_e32 v235, v91
	v_exp_f32_e32 v236, v92
	v_exp_f32_e32 v237, v93
	v_exp_f32_e32 v238, v94
	v_mfma_f32_32x32x16_bf16 v[64:79], v[68:71], v[122:125], 0
	v_exp_f32_e32 v95, v95
	s_waitcnt lgkmcnt(2)
	v_mfma_f32_32x32x16_bf16 v[96:111], v[200:203], v[126:129], v[96:111]
	v_mfma_f32_32x32x16_bf16 v[64:79], v[204:207], v[126:129], v[64:79]
	ds_read_b128 v[200:203], v133 offset:50176
	ds_read_b128 v[204:207], v133 offset:58368
	s_waitcnt lgkmcnt(2)
	v_mfma_f32_32x32x16_bf16 v[96:111], v[138:141], v[118:121], v[96:111]
	v_mfma_f32_32x32x16_bf16 v[64:79], v[142:145], v[118:121], v[64:79]
	s_waitcnt lgkmcnt(0)
	v_mfma_f32_32x32x16_bf16 v[96:111], v[200:203], v[114:117], v[96:111]
	v_exp_f32_e32 v201, v80
	v_add_f32_e32 v80, v208, v197
	v_add_f32_e32 v199, v209, v210
	v_add_f32_e32 v80, v211, v80
	v_add_f32_e32 v199, v220, v199
	v_add_f32_e32 v80, v221, v80
	v_add_f32_e32 v199, v222, v199
	v_add_f32_e32 v80, v223, v80
	v_add_f32_e32 v199, v224, v199
	v_add_f32_e32 v80, v225, v80
	v_add_f32_e32 v199, v226, v199
	v_add_f32_e32 v80, v227, v80
	v_exp_f32_e32 v202, v81
	v_add_f32_e32 v199, v228, v199
	v_exp_f32_e32 v203, v82
	v_add_f32_e32 v80, v229, v80
	v_mfma_f32_32x32x16_bf16 v[64:79], v[204:207], v[114:117], v[64:79]
	v_exp_f32_e32 v204, v83
	v_add_f32_e32 v199, v230, v199
	v_exp_f32_e32 v205, v84
	v_add_f32_e32 v80, v201, v80
	v_exp_f32_e32 v206, v85
	v_add_f32_e32 v199, v202, v199
	v_exp_f32_e32 v207, v86
	v_add_f32_e32 v80, v203, v80
	v_add_f32_e32 v199, v204, v199
	v_add_f32_e32 v80, v205, v80
	v_add_f32_e32 v199, v206, v199
	v_add_f32_e32 v80, v207, v80
	v_add_f32_e32 v199, v231, v199
	v_add_f32_e32 v80, v232, v80
	v_add_f32_e32 v199, v233, v199
	v_add_f32_e32 v80, v234, v80
	v_add_f32_e32 v199, v235, v199
	v_add_f32_e32 v80, v236, v80
	v_add_f32_e32 v199, v237, v199
	v_add_f32_e32 v80, v238, v80
	v_add_f32_e32 v199, v95, v199
	v_add_f32_e32 v199, v199, v80
	v_cvt_pk_bf16_f32 v80, v197, v208
	v_cvt_pk_bf16_f32 v81, v209, v210
	v_cvt_pk_bf16_f32 v82, v211, v220
	v_cvt_pk_bf16_f32 v83, v221, v222
	v_cvt_pk_bf16_f32 v84, v223, v224
	v_cvt_pk_bf16_f32 v85, v225, v226
	v_cvt_pk_bf16_f32 v86, v227, v228
	v_cvt_pk_bf16_f32 v87, v229, v230
	v_cvt_pk_bf16_f32 v88, v201, v202
	v_cvt_pk_bf16_f32 v89, v203, v204
	v_cvt_pk_bf16_f32 v90, v205, v206
	v_cvt_pk_bf16_f32 v91, v207, v231
	v_cvt_pk_bf16_f32 v92, v232, v233
	v_cvt_pk_bf16_f32 v93, v234, v235
	v_cvt_pk_bf16_f32 v94, v236, v237
	v_cvt_pk_bf16_f32 v95, v238, v95
	s_add_i32 m0, s84, 0x4400
	s_add_u32 s66, s78, s65
	s_addc_u32 s67, s79, 0
	global_load_lds_dwordx4 v185, s[66:67]
	s_add_i32 m0, s84, 0x6400
	s_add_i32 s64, s65, 0x60000
	global_load_lds_dwordx4 v184, s[66:67]
	s_cmp_eq_u32 s55, 29
	s_cselect_b32 s64, s89, s64
	s_add_i32 m0, s84, 0x14400
	s_add_u32 s70, s80, s64
	s_addc_u32 s71, s81, 0
	global_load_lds_dwordx4 v183, s[70:71]
	s_add_i32 m0, s84, 0x16400
	s_mov_b32 s65, s64
	global_load_lds_dwordx4 v182, s[70:71]
